# e10
# speedup vs baseline: 1.0409x; 1.0108x over previous
.LBB6_26:
	s_lshl_b64 s[0:1], s[6:7], 11
	v_lshl_add_u64 v[0:1], v[160:161], 0, s[0:1]
	s_or_b32 s0, s6, 1
	s_mov_b32 s1, 0
	s_waitcnt vmcnt(0)
	s_waitcnt lgkmcnt(0)
	s_barrier
	v_mov_b32_e32 v112, v232
	v_mov_b32_e32 v113, v233
	v_mov_b32_e32 v114, v234
	v_mov_b32_e32 v115, v235
	s_lshl_b64 s[2:3], s[0:1], 11
	v_lshl_add_u64 v[2:3], v[160:161], 0, s[2:3]
	v_mov_b32_e32 v116, v240
	v_mov_b32_e32 v117, v241
	v_mov_b32_e32 v118, v242
	v_mov_b32_e32 v119, v243
	v_mov_b32_e32 v120, v236
	v_mov_b32_e32 v121, v237
	v_mov_b32_e32 v122, v238
	v_mov_b32_e32 v123, v239
	v_mov_b32_e32 v124, v244
	v_mov_b32_e32 v125, v245
	v_mov_b32_e32 v126, v246
	v_mov_b32_e32 v127, v247
	v_add_co_u32_e32 v0, vcc, 0x10000, v160
	s_mov_b32 s2, 0x3f803f80
	s_nop 0
	v_addc_co_u32_e32 v1, vcc, 0, v161, vcc
	global_load_dwordx4 v[104:107], v[0:1], off
	global_load_dwordx4 v[100:103], v[0:1], off offset:1024
	ds_read_b128 v[136:139], v158
	ds_read_b128 v[132:135], v158 offset:1024
	v_mov_b32_e32 v0, 0
	s_mov_b32 s3, s2
	v_mov_b32_e32 v1, v0
	v_mov_b32_e32 v2, v0
	v_mov_b32_e32 v3, v0
	v_mov_b32_e32 v4, v0
	v_mov_b32_e32 v5, v0
	v_mov_b32_e32 v6, v0
	v_mov_b32_e32 v7, v0
	v_mov_b32_e32 v8, v0
	v_mov_b32_e32 v9, v0
	v_mov_b32_e32 v10, v0
	v_mov_b32_e32 v11, v0
	v_mov_b32_e32 v12, v0
	v_mov_b32_e32 v13, v0
	v_mov_b32_e32 v14, v0
	v_mov_b32_e32 v15, v0
	v_mov_b32_e32 v16, v0
	v_mov_b32_e32 v17, v0
	v_mov_b32_e32 v18, v0
	v_mov_b32_e32 v19, v0
	v_mov_b32_e32 v20, v0
	v_mov_b32_e32 v21, v0
	v_mov_b32_e32 v22, v0
	v_mov_b32_e32 v23, v0
	v_mov_b32_e32 v24, v0
	v_mov_b32_e32 v25, v0
	v_mov_b32_e32 v26, v0
	v_mov_b32_e32 v27, v0
	v_mov_b32_e32 v28, v0
	v_mov_b32_e32 v29, v0
	v_mov_b32_e32 v30, v0
	v_mov_b32_e32 v31, v0
	v_mov_b64_e32 v[96:97], s[2:3]
	v_mov_b32_e32 v144, v0
	v_mov_b32_e32 v145, v0
	v_mov_b32_e32 v146, v0
	v_mov_b32_e32 v147, v0
	v_mov_b32_e32 v140, v0
	v_mov_b32_e32 v141, v0
	v_mov_b32_e32 v142, v0
	v_mov_b32_e32 v143, v0
	s_waitcnt vmcnt(5) lgkmcnt(1)
	v_mfma_f32_32x32x16_bf16 v[48:63], v[136:139], v[112:115], 0
	s_waitcnt vmcnt(4)
	v_mfma_f32_32x32x16_bf16 v[32:47], v[136:139], v[116:119], 0
	s_waitcnt vmcnt(3) lgkmcnt(0)
	v_mfma_f32_32x32x16_bf16 v[48:63], v[132:135], v[120:123], v[48:63]
	s_waitcnt vmcnt(2)
	v_mfma_f32_32x32x16_bf16 v[32:47], v[132:135], v[124:127], v[32:47]
	v_mov_b32_e32 v180, v0
	v_mov_b32_e32 v181, v0
	v_mov_b32_e32 v182, v0
	v_mov_b32_e32 v183, v0
	v_mov_b32_e32 v184, v0
	v_mov_b32_e32 v185, v0
	v_mov_b32_e32 v186, v0
	v_mov_b32_e32 v187, v0
	v_mov_b32_e32 v76, v0
	v_mov_b32_e32 v77, v0
	v_mov_b32_e32 v78, v0
	v_mov_b32_e32 v79, v0
	v_mov_b32_e32 v168, v0
	v_mov_b32_e32 v169, v0
	v_mov_b32_e32 v170, v0
	v_mov_b32_e32 v171, v0
	v_mov_b32_e32 v248, v0
	v_mov_b32_e32 v249, v0
	v_mov_b32_e32 v250, v0
	v_mov_b32_e32 v251, v0
	ds_read_b128 v[196:199], v158 offset:2048
	ds_read_b128 v[108:111], v158 offset:3072
	s_nop 0
	s_cmp_lt_u32 s31, 4
	s_cbranch_scc1 .Lmy_prio1
	s_setprio 1
.Lmy_prio1:
.Lmy_attn_loop1:
	v_add_u32_e32 v252, s1, v158
	v_add_u32_e32 v253, 0x10800, v252
	s_waitcnt lgkmcnt(0)
	v_mfma_f32_32x32x16_bf16 v[80:95], v[196:199], v[112:115], 0
	ds_read_b128 v[128:131], v253 offset:0
	ds_read_b128 v[148:151], v253 offset:1024
	v_cvt_pk_bf16_f32 v186, v76, v77
	v_cvt_pk_bf16_f32 v187, v78, v79
	v_exp_f32_e32 v48, v48
	v_exp_f32_e32 v49, v49
	v_exp_f32_e32 v50, v50
	v_exp_f32_e32 v51, v51
	v_mfma_f32_4x4x4_16b_bf16 v[140:143], v[96:97], v[180:181], v[140:143]
	v_mfma_f32_32x32x16_bf16 v[80:95], v[108:111], v[120:123], v[80:95]
	v_exp_f32_e32 v52, v52
	v_exp_f32_e32 v53, v53
	v_exp_f32_e32 v54, v54
	v_exp_f32_e32 v55, v55
	v_cvt_pk_bf16_f32 v172, v48, v49
	v_cvt_pk_bf16_f32 v173, v50, v51
	v_mfma_f32_4x4x4_16b_bf16 v[140:143], v[96:97], v[182:183], v[140:143]
	v_mfma_f32_32x32x16_bf16 v[0:15], v[168:171], v[180:183], v[0:15]
	v_exp_f32_e32 v56, v56
	v_exp_f32_e32 v57, v57
	v_exp_f32_e32 v58, v58
	v_exp_f32_e32 v59, v59
	v_cvt_pk_bf16_f32 v174, v52, v53
	v_cvt_pk_bf16_f32 v175, v54, v55
	v_mfma_f32_4x4x4_16b_bf16 v[140:143], v[96:97], v[184:185], v[140:143]
	v_mfma_f32_32x32x16_bf16 v[0:15], v[248:251], v[184:187], v[0:15]
	v_exp_f32_e32 v60, v60
	v_exp_f32_e32 v61, v61
	v_exp_f32_e32 v62, v62
	v_exp_f32_e32 v63, v63
	v_cvt_pk_bf16_f32 v176, v56, v57
	v_cvt_pk_bf16_f32 v177, v58, v59
	v_mfma_f32_4x4x4_16b_bf16 v[140:143], v[96:97], v[186:187], v[140:143]
	v_mfma_f32_32x32x16_bf16 v[64:79], v[196:199], v[116:119], 0
	ds_read_b128 v[188:191], v252 offset:4096
	ds_read_b128 v[192:195], v252 offset:5120
	v_cvt_pk_bf16_f32 v178, v60, v61
	v_cvt_pk_bf16_f32 v179, v62, v63
	v_exp_f32_e32 v32, v32
	v_exp_f32_e32 v33, v33
	v_exp_f32_e32 v34, v34
	v_exp_f32_e32 v35, v35
	v_mfma_f32_4x4x4_16b_bf16 v[144:147], v[96:97], v[172:173], v[144:147]
	v_mfma_f32_32x32x16_bf16 v[64:79], v[108:111], v[124:127], v[64:79]
	v_exp_f32_e32 v36, v36
	v_exp_f32_e32 v37, v37
	v_exp_f32_e32 v38, v38
	v_exp_f32_e32 v39, v39
	v_cvt_pk_bf16_f32 v180, v32, v33
	v_cvt_pk_bf16_f32 v181, v34, v35
	v_mfma_f32_4x4x4_16b_bf16 v[144:147], v[96:97], v[174:175], v[144:147]
	s_waitcnt lgkmcnt(2)
	v_mfma_f32_32x32x16_bf16 v[16:31], v[128:131], v[172:175], v[16:31]
	v_exp_f32_e32 v40, v40
	v_exp_f32_e32 v41, v41
	v_exp_f32_e32 v42, v42
	v_exp_f32_e32 v43, v43
	v_cvt_pk_bf16_f32 v182, v36, v37
	v_cvt_pk_bf16_f32 v183, v38, v39
	v_mfma_f32_4x4x4_16b_bf16 v[144:147], v[96:97], v[176:177], v[144:147]
	v_mfma_f32_32x32x16_bf16 v[16:31], v[148:151], v[176:179], v[16:31]
	v_exp_f32_e32 v44, v44
	v_exp_f32_e32 v45, v45
	v_exp_f32_e32 v46, v46
	v_exp_f32_e32 v47, v47
	v_cvt_pk_bf16_f32 v184, v40, v41
	v_cvt_pk_bf16_f32 v185, v42, v43
	v_mfma_f32_4x4x4_16b_bf16 v[144:147], v[96:97], v[178:179], v[144:147]
	s_waitcnt lgkmcnt(0)
	v_mfma_f32_32x32x16_bf16 v[48:63], v[188:191], v[112:115], 0
	ds_read_b128 v[168:171], v253 offset:2048
	ds_read_b128 v[248:251], v253 offset:3072
	v_cvt_pk_bf16_f32 v186, v44, v45
	v_cvt_pk_bf16_f32 v187, v46, v47
	v_exp_f32_e32 v80, v80
	v_exp_f32_e32 v81, v81
	v_exp_f32_e32 v82, v82
	v_exp_f32_e32 v83, v83
	v_mfma_f32_4x4x4_16b_bf16 v[140:143], v[96:97], v[180:181], v[140:143]
	v_mfma_f32_32x32x16_bf16 v[48:63], v[192:195], v[120:123], v[48:63]
	v_exp_f32_e32 v84, v84
	v_exp_f32_e32 v85, v85
	v_exp_f32_e32 v86, v86
	v_exp_f32_e32 v87, v87
	v_cvt_pk_bf16_f32 v172, v80, v81
	v_cvt_pk_bf16_f32 v173, v82, v83
	v_mfma_f32_4x4x4_16b_bf16 v[140:143], v[96:97], v[182:183], v[140:143]
	v_mfma_f32_32x32x16_bf16 v[0:15], v[128:131], v[180:183], v[0:15]
	v_exp_f32_e32 v88, v88
	v_exp_f32_e32 v89, v89
	v_exp_f32_e32 v90, v90
	v_exp_f32_e32 v91, v91
	v_cvt_pk_bf16_f32 v174, v84, v85
	v_cvt_pk_bf16_f32 v175, v86, v87
	v_mfma_f32_4x4x4_16b_bf16 v[140:143], v[96:97], v[184:185], v[140:143]
	v_mfma_f32_32x32x16_bf16 v[0:15], v[148:151], v[184:187], v[0:15]
	v_exp_f32_e32 v92, v92
	v_exp_f32_e32 v93, v93
	v_exp_f32_e32 v94, v94
	v_exp_f32_e32 v95, v95
	v_cvt_pk_bf16_f32 v176, v88, v89
	v_cvt_pk_bf16_f32 v177, v90, v91
	v_mfma_f32_4x4x4_16b_bf16 v[140:143], v[96:97], v[186:187], v[140:143]
	v_mfma_f32_32x32x16_bf16 v[32:47], v[188:191], v[116:119], 0
	ds_read_b128 v[196:199], v252 offset:6144
	ds_read_b128 v[108:111], v252 offset:7168
	v_cvt_pk_bf16_f32 v178, v92, v93
	v_cvt_pk_bf16_f32 v179, v94, v95
	v_exp_f32_e32 v64, v64
	v_exp_f32_e32 v65, v65
	v_exp_f32_e32 v66, v66
	v_exp_f32_e32 v67, v67
	v_mfma_f32_4x4x4_16b_bf16 v[144:147], v[96:97], v[172:173], v[144:147]
	v_mfma_f32_32x32x16_bf16 v[32:47], v[192:195], v[124:127], v[32:47]
	v_exp_f32_e32 v68, v68
	v_exp_f32_e32 v69, v69
	v_exp_f32_e32 v70, v70
	v_exp_f32_e32 v71, v71
	v_cvt_pk_bf16_f32 v180, v64, v65
	v_cvt_pk_bf16_f32 v181, v66, v67
	v_mfma_f32_4x4x4_16b_bf16 v[144:147], v[96:97], v[174:175], v[144:147]
	s_waitcnt lgkmcnt(2)
	v_mfma_f32_32x32x16_bf16 v[16:31], v[168:171], v[172:175], v[16:31]
	v_exp_f32_e32 v72, v72
	v_exp_f32_e32 v73, v73
	v_exp_f32_e32 v74, v74
	v_exp_f32_e32 v75, v75
	v_cvt_pk_bf16_f32 v182, v68, v69
	v_cvt_pk_bf16_f32 v183, v70, v71
	v_mfma_f32_4x4x4_16b_bf16 v[144:147], v[96:97], v[176:177], v[144:147]
	v_mfma_f32_32x32x16_bf16 v[16:31], v[248:251], v[176:179], v[16:31]
	v_exp_f32_e32 v76, v76
	v_exp_f32_e32 v77, v77
	v_exp_f32_e32 v78, v78
	v_exp_f32_e32 v79, v79
	v_cvt_pk_bf16_f32 v184, v72, v73
	v_cvt_pk_bf16_f32 v185, v74, v75
	v_mfma_f32_4x4x4_16b_bf16 v[144:147], v[96:97], v[178:179], v[144:147]
	s_addk_i32 s1, 0x1000
	s_cmp_lg_u32 s1, 0x10000
	s_cbranch_scc1 .Lmy_attn_loop1
	v_cvt_pk_bf16_f32 v186, v76, v77
	v_cvt_pk_bf16_f32 v187, v78, v79
	v_mfma_f32_4x4x4_16b_bf16 v[140:143], v[96:97], v[180:181], v[140:143]
	v_mfma_f32_32x32x16_bf16 v[0:15], v[168:171], v[180:183], v[0:15]
	s_nop 0
	v_mfma_f32_4x4x4_16b_bf16 v[140:143], v[96:97], v[182:183], v[140:143]
	v_mfma_f32_32x32x16_bf16 v[0:15], v[248:251], v[184:187], v[0:15]
	s_nop 0
	v_mfma_f32_4x4x4_16b_bf16 v[140:143], v[96:97], v[184:185], v[140:143]
	s_nop 1
	v_mfma_f32_4x4x4_16b_bf16 v[140:143], v[96:97], v[186:187], v[140:143]
	v_mov_b32_e32 v34, 0x3f80
	v_cmp_gt_u32_e64 s[0:1], 32, v154
	v_or_b32_e32 v36, 0x20c00, v158
	s_mov_b32 s2, 0x3f803f80
	v_cndmask_b32_e64 v96, 0, v34, s[0:1]
	v_or_b32_e32 v34, 0x20800, v158
	ds_read_b128 v[108:111], v34
	ds_read_b128 v[128:131], v36
	v_exp_f32_e32 v34, v48
	v_exp_f32_e32 v35, v49
	s_mov_b32 s3, s2
	v_mov_b64_e32 v[52:53], s[2:3]
	v_exp_f32_e32 v32, v32
	v_exp_f32_e32 v33, v33
	v_mov_b32_e32 v97, 0
	v_cndmask_b32_e64 v34, 0, v34, s[0:1]
	v_cndmask_b32_e64 v35, 0, v35, s[0:1]
	v_cvt_pk_bf16_f32 v34, v34, v35
	v_mov_b32_e32 v35, v97
	v_mov_b32_e32 v36, v97
	v_mov_b32_e32 v37, v97
	s_mov_b32 s8, 0
	v_cndmask_b32_e64 v32, 0, v32, s[0:1]
	v_cndmask_b32_e64 v33, 0, v33, s[0:1]
	s_waitcnt lgkmcnt(1)
	v_mfma_f32_32x32x16_bf16 v[16:31], v[108:111], v[34:37], v[16:31]
	s_mov_b32 s9, s8
	v_cvt_pk_bf16_f32 v46, v32, v33
	v_mov_b64_e32 v[50:51], s[8:9]
	v_mov_b32_e32 v32, v46
	v_mov_b32_e32 v33, v97
	v_mov_b32_e32 v47, v97
	v_mov_b32_e32 v48, v97
	v_mfma_f32_4x4x4_16b_bf16 v[34:37], v[52:53], v[34:35], v[144:147]
	v_mov_b32_e32 v49, v97
	s_mov_b32 s10, s8
	v_mfma_f32_4x4x4_16b_bf16 v[38:41], v[52:53], v[50:51], v[34:37]
	s_mov_b32 s11, s8
	v_mfma_f32_4x4x4_16b_bf16 v[32:35], v[52:53], v[32:33], v[140:143]
	v_mov_b64_e32 v[44:45], s[10:11]
	v_mfma_f32_32x32x16_bf16 v[0:15], v[108:111], v[46:49], v[0:15]
	v_mov_b64_e32 v[42:43], s[8:9]
	s_mov_b32 s7, 0x7149f2ca
	s_mov_b32 s4, 0xda24260
	v_mov_b32_e32 v98, v97
	v_mov_b32_e32 v99, v97
	v_mfma_f32_4x4x4_16b_bf16 v[32:35], v[52:53], v[50:51], v[32:35]
	s_waitcnt lgkmcnt(0)
	v_mfma_f32_32x32x16_bf16 v[16:31], v[128:131], v[42:45], v[16:31]
	s_nop 2
	v_mbcnt_lo_u32_b32 v33, -1, 0
	v_mbcnt_hi_u32_b32 v33, -1, v33
	v_and_b32_e32 v35, 64, v33
	v_xor_b32_e32 v34, 32, v33
	v_add_u32_e32 v35, 64, v35
	v_cmp_lt_i32_e32 vcc, v34, v35
	v_mfma_f32_32x32x16_bf16 v[0:15], v[128:131], v[42:45], v[0:15]
	s_nop 0
	v_cndmask_b32_e32 v33, v33, v34, vcc
	v_lshlrev_b32_e32 v165, 2, v33
	ds_bpermute_b32 v35, v165, v38
	ds_bpermute_b32 v34, v165, v32
	v_mov_b32_e32 v33, v38
	s_waitcnt lgkmcnt(0)
	v_pk_add_f32 v[34:35], v[32:33], v[34:35]
	s_nop 0
	v_cmp_ngt_f32_e32 vcc, s7, v35
	v_cmp_nlt_f32_e64 s[2:3], s4, v34
	v_cmp_nlt_f32_e64 s[4:5], s4, v35
	s_or_b64 s[4:5], s[4:5], vcc
	v_cmp_ngt_f32_e32 vcc, s7, v34
	s_or_b64 s[2:3], s[2:3], vcc
	s_or_b64 vcc, s[4:5], s[2:3]
	s_cbranch_vccnz .LBB6_40

.LBB6_34:
	s_or_b64 exec, exec, s[4:5]
	s_or_b32 s26, s6, 2
	s_mov_b32 s27, 0
	s_lshl_b64 s[4:5], s[26:27], 11
	s_waitcnt lgkmcnt(0)
	v_lshl_add_u64 v[0:1], v[160:161], 0, s[4:5]
	s_or_b32 s4, s6, 3
	s_mov_b32 s5, s27
	v_mov_b32_e32 v100, v216
	v_mov_b32_e32 v101, v217
	v_mov_b32_e32 v102, v218
	v_mov_b32_e32 v103, v219
	s_lshl_b64 s[4:5], s[4:5], 11
	v_lshl_add_u64 v[2:3], v[160:161], 0, s[4:5]
	v_mov_b32_e32 v104, v224
	v_mov_b32_e32 v105, v225
	v_mov_b32_e32 v106, v226
	v_mov_b32_e32 v107, v227
	v_mov_b32_e32 v108, v220
	v_mov_b32_e32 v109, v221
	v_mov_b32_e32 v110, v222
	v_mov_b32_e32 v111, v223
	v_mov_b32_e32 v112, v228
	v_mov_b32_e32 v113, v229
	v_mov_b32_e32 v114, v230
	v_mov_b32_e32 v115, v231
	ds_read_b128 v[132:135], v158
	ds_read_b128 v[128:131], v158 offset:1024
	s_mov_b32 s4, 0x3f803f80
	v_mov_b32_e32 v136, 0
	s_mov_b32 s5, s4
	v_mov_b32_e32 v137, v136
	v_mov_b32_e32 v138, v136
	v_mov_b32_e32 v139, v136
	v_mov_b32_e32 v140, v136
	v_mov_b32_e32 v141, v136
	v_mov_b32_e32 v142, v136
	v_mov_b32_e32 v143, v136
	v_mov_b32_e32 v0, v136
	v_mov_b32_e32 v1, v136
	v_mov_b32_e32 v2, v136
	v_mov_b32_e32 v3, v136
	v_mov_b32_e32 v4, v136
	v_mov_b32_e32 v5, v136
	v_mov_b32_e32 v6, v136
	v_mov_b32_e32 v7, v136
	v_mov_b32_e32 v8, v136
	v_mov_b32_e32 v9, v136
	v_mov_b32_e32 v10, v136
	v_mov_b32_e32 v11, v136
	v_mov_b32_e32 v12, v136
	v_mov_b32_e32 v13, v136
	v_mov_b32_e32 v14, v136
	v_mov_b32_e32 v15, v136
	v_mov_b32_e32 v16, v136
	v_mov_b32_e32 v17, v136
	v_mov_b32_e32 v18, v136
	v_mov_b32_e32 v19, v136
	v_mov_b32_e32 v20, v136
	v_mov_b32_e32 v21, v136
	v_mov_b32_e32 v22, v136
	v_mov_b32_e32 v23, v136
	v_mov_b64_e32 v[116:117], s[4:5]
	v_mov_b32_e32 v24, v136
	v_mov_b32_e32 v25, v136
	v_mov_b32_e32 v26, v136
	v_mov_b32_e32 v27, v136
	v_mov_b32_e32 v28, v136
	v_mov_b32_e32 v29, v136
	v_mov_b32_e32 v30, v136
	v_mov_b32_e32 v31, v136
	s_waitcnt vmcnt(3) lgkmcnt(1)
	v_mfma_f32_32x32x16_bf16 v[48:63], v[132:135], v[100:103], 0
	s_waitcnt vmcnt(2)
	v_mfma_f32_32x32x16_bf16 v[32:47], v[132:135], v[104:107], 0
	s_waitcnt vmcnt(1) lgkmcnt(0)
	v_mfma_f32_32x32x16_bf16 v[48:63], v[128:131], v[108:111], v[48:63]
	s_waitcnt vmcnt(0)
	v_mfma_f32_32x32x16_bf16 v[32:47], v[128:131], v[112:115], v[32:47]
	v_mov_b32_e32 v180, v136
	v_mov_b32_e32 v181, v136
	v_mov_b32_e32 v182, v136
	v_mov_b32_e32 v183, v136
	v_mov_b32_e32 v184, v136
	v_mov_b32_e32 v185, v136
	v_mov_b32_e32 v186, v136
	v_mov_b32_e32 v187, v136
	v_mov_b32_e32 v76, v136
	v_mov_b32_e32 v77, v136
	v_mov_b32_e32 v78, v136
	v_mov_b32_e32 v79, v136
	v_mov_b32_e32 v240, v136
	v_mov_b32_e32 v241, v136
	v_mov_b32_e32 v242, v136
	v_mov_b32_e32 v243, v136
	v_mov_b32_e32 v244, v136
	v_mov_b32_e32 v245, v136
	v_mov_b32_e32 v246, v136
	v_mov_b32_e32 v247, v136
	ds_read_b128 v[224:227], v158 offset:2048
	ds_read_b128 v[228:231], v158 offset:3072
	s_nop 0
	s_setprio 0
	s_cmp_lt_u32 s31, 4
	s_cbranch_scc0 .Lmy_prio2
	s_setprio 1
.Lmy_prio2:
.Lmy_attn_loop2:
	v_add_u32_e32 v248, s27, v158
	v_add_u32_e32 v249, 0x10800, v248
	s_waitcnt lgkmcnt(0)
	v_mfma_f32_32x32x16_bf16 v[80:95], v[224:227], v[100:103], 0
	ds_read_b128 v[232:235], v249 offset:0
	ds_read_b128 v[236:239], v249 offset:1024
	v_cvt_pk_bf16_f32 v186, v76, v77
	v_cvt_pk_bf16_f32 v187, v78, v79
	v_exp_f32_e32 v48, v48
	v_exp_f32_e32 v49, v49
	v_exp_f32_e32 v50, v50
	v_exp_f32_e32 v51, v51
	v_mfma_f32_4x4x4_16b_bf16 v[136:139], v[116:117], v[180:181], v[136:139]
	v_mfma_f32_32x32x16_bf16 v[80:95], v[228:231], v[108:111], v[80:95]
	v_exp_f32_e32 v52, v52
	v_exp_f32_e32 v53, v53
	v_exp_f32_e32 v54, v54
	v_exp_f32_e32 v55, v55
	v_cvt_pk_bf16_f32 v172, v48, v49
	v_cvt_pk_bf16_f32 v173, v50, v51
	v_mfma_f32_4x4x4_16b_bf16 v[136:139], v[116:117], v[182:183], v[136:139]
	v_mfma_f32_32x32x16_bf16 v[0:15], v[240:243], v[180:183], v[0:15]
	v_exp_f32_e32 v56, v56
	v_exp_f32_e32 v57, v57
	v_exp_f32_e32 v58, v58
	v_exp_f32_e32 v59, v59
	v_cvt_pk_bf16_f32 v174, v52, v53
	v_cvt_pk_bf16_f32 v175, v54, v55
	v_mfma_f32_4x4x4_16b_bf16 v[136:139], v[116:117], v[184:185], v[136:139]
	v_mfma_f32_32x32x16_bf16 v[0:15], v[244:247], v[184:187], v[0:15]
	v_exp_f32_e32 v60, v60
	v_exp_f32_e32 v61, v61
	v_exp_f32_e32 v62, v62
	v_exp_f32_e32 v63, v63
	v_cvt_pk_bf16_f32 v176, v56, v57
	v_cvt_pk_bf16_f32 v177, v58, v59
	v_mfma_f32_4x4x4_16b_bf16 v[136:139], v[116:117], v[186:187], v[136:139]
	v_mfma_f32_32x32x16_bf16 v[64:79], v[224:227], v[104:107], 0
	ds_read_b128 v[216:219], v248 offset:4096
	ds_read_b128 v[220:223], v248 offset:5120
	v_cvt_pk_bf16_f32 v178, v60, v61
	v_cvt_pk_bf16_f32 v179, v62, v63
	v_exp_f32_e32 v32, v32
	v_exp_f32_e32 v33, v33
	v_exp_f32_e32 v34, v34
	v_exp_f32_e32 v35, v35
	v_mfma_f32_4x4x4_16b_bf16 v[140:143], v[116:117], v[172:173], v[140:143]
	v_mfma_f32_32x32x16_bf16 v[64:79], v[228:231], v[112:115], v[64:79]
	v_exp_f32_e32 v36, v36
	v_exp_f32_e32 v37, v37
	v_exp_f32_e32 v38, v38
	v_exp_f32_e32 v39, v39
	v_cvt_pk_bf16_f32 v180, v32, v33
	v_cvt_pk_bf16_f32 v181, v34, v35
	v_mfma_f32_4x4x4_16b_bf16 v[140:143], v[116:117], v[174:175], v[140:143]
	s_waitcnt lgkmcnt(2)
	v_mfma_f32_32x32x16_bf16 v[16:31], v[232:235], v[172:175], v[16:31]
	v_exp_f32_e32 v40, v40
	v_exp_f32_e32 v41, v41
	v_exp_f32_e32 v42, v42
	v_exp_f32_e32 v43, v43
	v_cvt_pk_bf16_f32 v182, v36, v37
	v_cvt_pk_bf16_f32 v183, v38, v39
	v_mfma_f32_4x4x4_16b_bf16 v[140:143], v[116:117], v[176:177], v[140:143]
	v_mfma_f32_32x32x16_bf16 v[16:31], v[236:239], v[176:179], v[16:31]
	v_exp_f32_e32 v44, v44
	v_exp_f32_e32 v45, v45
	v_exp_f32_e32 v46, v46
	v_exp_f32_e32 v47, v47
	v_cvt_pk_bf16_f32 v184, v40, v41
	v_cvt_pk_bf16_f32 v185, v42, v43
	v_mfma_f32_4x4x4_16b_bf16 v[140:143], v[116:117], v[178:179], v[140:143]
	s_waitcnt lgkmcnt(0)
	v_mfma_f32_32x32x16_bf16 v[48:63], v[216:219], v[100:103], 0
	ds_read_b128 v[240:243], v249 offset:2048
	ds_read_b128 v[244:247], v249 offset:3072
	v_cvt_pk_bf16_f32 v186, v44, v45
	v_cvt_pk_bf16_f32 v187, v46, v47
	v_exp_f32_e32 v80, v80
	v_exp_f32_e32 v81, v81
	v_exp_f32_e32 v82, v82
	v_exp_f32_e32 v83, v83
	v_mfma_f32_4x4x4_16b_bf16 v[136:139], v[116:117], v[180:181], v[136:139]
	v_mfma_f32_32x32x16_bf16 v[48:63], v[220:223], v[108:111], v[48:63]
	v_exp_f32_e32 v84, v84
	v_exp_f32_e32 v85, v85
	v_exp_f32_e32 v86, v86
	v_exp_f32_e32 v87, v87
	v_cvt_pk_bf16_f32 v172, v80, v81
	v_cvt_pk_bf16_f32 v173, v82, v83
	v_mfma_f32_4x4x4_16b_bf16 v[136:139], v[116:117], v[182:183], v[136:139]
	v_mfma_f32_32x32x16_bf16 v[0:15], v[232:235], v[180:183], v[0:15]
	v_exp_f32_e32 v88, v88
	v_exp_f32_e32 v89, v89
	v_exp_f32_e32 v90, v90
	v_exp_f32_e32 v91, v91
	v_cvt_pk_bf16_f32 v174, v84, v85
	v_cvt_pk_bf16_f32 v175, v86, v87
	v_mfma_f32_4x4x4_16b_bf16 v[136:139], v[116:117], v[184:185], v[136:139]
	v_mfma_f32_32x32x16_bf16 v[0:15], v[236:239], v[184:187], v[0:15]
	v_exp_f32_e32 v92, v92
	v_exp_f32_e32 v93, v93
	v_exp_f32_e32 v94, v94
	v_exp_f32_e32 v95, v95
	v_cvt_pk_bf16_f32 v176, v88, v89
	v_cvt_pk_bf16_f32 v177, v90, v91
	v_mfma_f32_4x4x4_16b_bf16 v[136:139], v[116:117], v[186:187], v[136:139]
	v_mfma_f32_32x32x16_bf16 v[32:47], v[216:219], v[104:107], 0
	ds_read_b128 v[224:227], v248 offset:6144
	ds_read_b128 v[228:231], v248 offset:7168
	v_cvt_pk_bf16_f32 v178, v92, v93
	v_cvt_pk_bf16_f32 v179, v94, v95
	v_exp_f32_e32 v64, v64
	v_exp_f32_e32 v65, v65
	v_exp_f32_e32 v66, v66
	v_exp_f32_e32 v67, v67
	v_mfma_f32_4x4x4_16b_bf16 v[140:143], v[116:117], v[172:173], v[140:143]
	v_mfma_f32_32x32x16_bf16 v[32:47], v[220:223], v[112:115], v[32:47]
	v_exp_f32_e32 v68, v68
	v_exp_f32_e32 v69, v69
	v_exp_f32_e32 v70, v70
	v_exp_f32_e32 v71, v71
	v_cvt_pk_bf16_f32 v180, v64, v65
	v_cvt_pk_bf16_f32 v181, v66, v67
	v_mfma_f32_4x4x4_16b_bf16 v[140:143], v[116:117], v[174:175], v[140:143]
	s_waitcnt lgkmcnt(2)
	v_mfma_f32_32x32x16_bf16 v[16:31], v[240:243], v[172:175], v[16:31]
	v_exp_f32_e32 v72, v72
	v_exp_f32_e32 v73, v73
	v_exp_f32_e32 v74, v74
	v_exp_f32_e32 v75, v75
	v_cvt_pk_bf16_f32 v182, v68, v69
	v_cvt_pk_bf16_f32 v183, v70, v71
	v_mfma_f32_4x4x4_16b_bf16 v[140:143], v[116:117], v[176:177], v[140:143]
	v_mfma_f32_32x32x16_bf16 v[16:31], v[244:247], v[176:179], v[16:31]
	v_exp_f32_e32 v76, v76
	v_exp_f32_e32 v77, v77
	v_exp_f32_e32 v78, v78
	v_exp_f32_e32 v79, v79
	v_cvt_pk_bf16_f32 v184, v72, v73
	v_cvt_pk_bf16_f32 v185, v74, v75
	v_mfma_f32_4x4x4_16b_bf16 v[140:143], v[116:117], v[178:179], v[140:143]
	s_addk_i32 s27, 0x1000
	s_cmp_lg_u32 s27, 0x10000
	s_cbranch_scc1 .Lmy_attn_loop2
	v_cvt_pk_bf16_f32 v186, v76, v77
	v_cvt_pk_bf16_f32 v187, v78, v79
	v_mfma_f32_4x4x4_16b_bf16 v[136:139], v[116:117], v[180:181], v[136:139]
	v_mfma_f32_32x32x16_bf16 v[0:15], v[240:243], v[180:183], v[0:15]
	s_nop 0
	v_mfma_f32_4x4x4_16b_bf16 v[136:139], v[116:117], v[182:183], v[136:139]
	v_mfma_f32_32x32x16_bf16 v[0:15], v[244:247], v[184:187], v[0:15]
	s_nop 0
	v_mfma_f32_4x4x4_16b_bf16 v[136:139], v[116:117], v[184:185], v[136:139]
	s_nop 1
	v_mfma_f32_4x4x4_16b_bf16 v[136:139], v[116:117], v[186:187], v[136:139]
	s_setprio 0
	v_or_b32_e32 v34, 0x20800, v158
	ds_read_b128 v[116:119], v34
	v_or_b32_e32 v36, 0x20c00, v158
	s_mov_b32 s4, 0x3f803f80
	v_exp_f32_e32 v35, v49
	ds_read_b128 v[120:123], v36
	v_exp_f32_e32 v34, v48
	s_mov_b32 s5, s4
	v_mov_b64_e32 v[46:47], s[4:5]
	v_exp_f32_e32 v38, v32
	v_exp_f32_e32 v39, v33
	v_cndmask_b32_e64 v34, 0, v34, s[0:1]
	v_cndmask_b32_e64 v35, 0, v35, s[0:1]
	v_mov_b32_e32 v125, 0
	v_cvt_pk_bf16_f32 v124, v34, v35
	v_mov_b32_e32 v126, v125
	v_mov_b32_e32 v127, v125
	v_cndmask_b32_e64 v38, 0, v38, s[0:1]
	v_cndmask_b32_e64 v39, 0, v39, s[0:1]
	s_waitcnt lgkmcnt(1)
	v_mfma_f32_32x32x16_bf16 v[16:31], v[116:119], v[124:127], v[16:31]
	s_mov_b32 s8, 0
	s_mov_b32 s9, s8
	v_mov_b64_e32 v[36:37], s[8:9]
	s_mov_b32 s10, s8
	s_mov_b32 s11, s8
	v_mov_b64_e32 v[44:45], s[10:11]
	v_mov_b64_e32 v[42:43], s[8:9]
	v_mfma_f32_4x4x4_16b_bf16 v[32:35], v[46:47], v[124:125], v[140:143]
	v_cvt_pk_bf16_f32 v124, v38, v39
	s_waitcnt lgkmcnt(0)
	v_mfma_f32_32x32x16_bf16 v[16:31], v[120:123], v[42:45], v[16:31]
	s_mov_b32 s9, 0x7149f2ca
	s_mov_b32 s6, 0xda24260
	v_mfma_f32_32x32x16_bf16 v[0:15], v[116:119], v[124:127], v[0:15]
	v_mfma_f32_4x4x4_16b_bf16 v[38:41], v[46:47], v[36:37], v[32:35]
	v_mfma_f32_4x4x4_16b_bf16 v[32:35], v[46:47], v[124:125], v[136:139]
	v_mfma_f32_32x32x16_bf16 v[0:15], v[120:123], v[42:45], v[0:15]
	s_nop 0
	v_mfma_f32_4x4x4_16b_bf16 v[32:35], v[46:47], v[36:37], v[32:35]
	s_nop 4
	ds_bpermute_b32 v35, v165, v38
	ds_bpermute_b32 v34, v165, v32
	v_mov_b32_e32 v33, v38
	s_waitcnt lgkmcnt(0)
	v_pk_add_f32 v[34:35], v[32:33], v[34:35]
	s_nop 0
	v_cmp_ngt_f32_e32 vcc, s9, v35
	v_cmp_nlt_f32_e64 s[4:5], s6, v34
	v_cmp_nlt_f32_e64 s[6:7], s6, v35
	s_or_b64 s[6:7], s[6:7], vcc
	v_cmp_ngt_f32_e32 vcc, s9, v34
	s_or_b64 s[4:5], s[4:5], vcc
	s_or_b64 vcc, s[6:7], s[4:5]
	s_cbranch_vccnz .LBB6_64
